# S5 final: the nine C-matrix fragments loaded once per state group with the group's other loads instead of inside each half's load->wait->MFMA chain (plus the conv-row load hoists)
# speedup vs baseline: 1.0062x; 1.0018x over previous
; #define LAS __attribute__((address_space(3)))
; template <bool FINAL>
; __device__ __forceinline__ void s5_group(int lane, const unsigned char* tab, const bf16* __restrict__ proj, f32x2* E, int c, int g, LAS bf16* sbuf, LAS bf16* yg) {
;     const int r32 = lane & 31, hi = lane >> 5;
;     const f32x2* abar = (const f32x2*)(tab + S5T_ABAR);
;     const bf16* bmat = (const bf16*)(tab + S5T_BMAT) + (size_t)g * 128 * 16; const bf16* cmat = (const bf16*)(tab + S5T_CMAT) + (size_t)g * 32 * CM_PITCH;
;     const f32x2 a0 = abar[g * 64 + r32], a1 = abar[g * 64 + 32 + r32];
;     bf16x8 bfr[4];
; #pragma unroll
;     for (int pt = 0; pt < 4; ++pt) bfr[pt] = *(const bf16x8*)(bmat + (32 * pt + r32) * 16 + 8 * hi);
;     float c0r = 0.f, c0i = 0.f, c1r = 0.f, c1i = 0.f;
;     if (FINAL) { const f32x2 v0 = E[((size_t)c * 32 + g) * 64 + r32], v1 = E[((size_t)c * 32 + g) * 64 + 32 + r32]; c0r = v0.x; c0i = v0.y; c1r = v1.x; c1i = v1.y; }
;     const int tok0 = 64 * c + 16 * ((r32 >> 2) & 1) + 4 * (r32 >> 3) + (r32 & 3);
;     const bf16x8 ufr0 = *(const bf16x8*)(proj + (size_t)tok0 * PW + C_S5U + 16 * g + 8 * hi), ufr1 = *(const bf16x8*)(proj + (size_t)(tok0 + 32) * PW + C_S5U + 16 * g + 8 * hi);
;     bf16x8 dfr0 = ufr0, dfr1 = ufr1;
;     if (FINAL) { dfr0 = *(const bf16x8*)(proj + (size_t)(64 * c + r32) * PW + C_S5U + 16 * g + 8 * hi); dfr1 = *(const bf16x8*)(proj + (size_t)(64 * c + 32 + r32) * PW + C_S5U + 16 * g + 8 * hi); }
.LBB0_652:
	s_add_i32 s10, s30, s15
	v_mad_i64_i32 v[116:117], s[34:35], s10, v254, v[110:111]
	global_load_dwordx4 v[164:167], v[116:117], off
	global_load_dwordx4 v[168:171], v[116:117], off offset:32
	global_load_dwordx4 v[172:175], v[116:117], off offset:64
	global_load_dwordx4 v[176:179], v[116:117], off offset:96
	global_load_dwordx4 v[180:183], v[116:117], off offset:128
	global_load_dwordx4 v[184:187], v[116:117], off offset:160
	global_load_dwordx4 v[188:191], v[116:117], off offset:192
	global_load_dwordx4 v[228:231], v[116:117], off offset:224
	global_load_dwordx4 v[232:235], v[116:117], off offset:256
	v_lshl_or_b32 v0, s10, 6, v124
	s_ashr_i32 s11, s10, 31
	v_ashrrev_i32_e32 v1, 31, v0
	s_lshl_b64 s[8:9], s[10:11], 12
	v_lshl_add_u64 v[0:1], v[0:1], 3, s[42:43]
	global_load_dwordx2 v[112:113], v[0:1], off
	global_load_dwordx2 v[114:115], v[0:1], off offset:256
	v_lshl_add_u64 v[0:1], v[98:99], 0, s[8:9]
	s_lshl_b64 s[8:9], s[10:11], 9
	v_lshl_add_u64 v[2:3], v[100:101], 0, s[8:9]
	s_lshl_b32 s8, s10, 4
	s_ashr_i32 s9, s8, 31
	s_lshl_b64 s[8:9], s[8:9], 1
	global_load_dwordx4 v[62:65], v[0:1], off
	global_load_dwordx4 v[66:69], v[0:1], off offset:1024
	global_load_dwordx4 v[70:73], v[0:1], off offset:2048
	global_load_dwordx4 v[74:77], v[0:1], off offset:3072
	s_nop 0
	global_load_dwordx2 v[0:1], v[2:3], off
	global_load_dwordx2 v[122:123], v[2:3], off offset:256
	v_lshl_add_u64 v[2:3], v[102:103], 0, s[8:9]
	v_lshl_add_u64 v[4:5], v[104:105], 0, s[8:9]
	global_load_dwordx4 v[78:81], v[2:3], off
	global_load_dwordx4 v[82:85], v[4:5], off
	v_lshl_add_u64 v[2:3], v[106:107], 0, s[8:9]
	v_lshl_add_u64 v[4:5], v[108:109], 0, s[8:9]
	global_load_dwordx4 v[86:89], v[2:3], off
	global_load_dwordx4 v[90:93], v[4:5], off
	s_mov_b64 s[8:9], -1
	v_lshl_add_u32 v129, s10, 5, v127
	s_mov_b32 s31, 0
	s_waitcnt vmcnt(11)
	v_pk_mov_b32 v[118:119], v[112:113], v[112:113] op_sel:[1,0]
	s_waitcnt vmcnt(10)
	v_pk_mov_b32 v[120:121], v[114:115], v[114:115] op_sel:[1,0]
	s_branch .LBB0_654

; __device__ __forceinline__ float partner32(float v, int hi) { float r0, r1; swap32(v, r0, r1); return hi ? r0 : r1; }
; __device__ __forceinline__ void scan16(f32x16& re, f32x16& im, float ar, float ai, float& cr, float& ci, int hi) {
;     float sr = hi ? 0.f : cr, si = hi ? 0.f : ci;
; #pragma unroll
;     for (int r = 0; r < 16; ++r) { const float nr = ar * sr - ai * si + re[r], ni = ar * si + ai * sr + im[r]; sr = nr; si = ni; re[r] = sr; im[r] = si; }
;     float xr = partner32(sr, hi), xi = partner32(si, hi);
;     xr = hi ? xr : 0.f; xi = hi ? xi : 0.f;
;     float pr = ar, pi = ai; asm volatile("" : "+v"(pr), "+v"(pi));
; #pragma unroll
;     for (int r = 0; r < 16; ++r) { re[r] += pr * xr - pi * xi; im[r] += pr * xi + pi * xr; const float t = pr * ar - pi * ai; pi = pr * ai + pi * ar; pr = t; }
;     const float er = partner32(re[15], hi), ei = partner32(im[15], hi);
;     cr = hi ? re[15] : er; ci = hi ? im[15] : ei;
; }
; template <bool FINAL>
; __device__ __forceinline__ void s5_group(int lane, const unsigned char* tab, const bf16* __restrict__ proj, f32x2* E, int c, int g, LAS bf16* sbuf, LAS bf16* yg) {
;     ...
;     for (int tt = 0; tt < 2; ++tt) {
;         const int t0 = 64 * c + 32 * tt;
;         const bf16x8 ufr = tt ? ufr1 : ufr0;
;         f32x16 acc[4];
; #pragma unroll
;         for (int pt = 0; pt < 4; ++pt) acc[pt] = __builtin_amdgcn_mfma_f32_32x32x16_bf16(ufr, bfr[pt], (f32x16){}, 0, 0, 0);
;         scan16(acc[0], acc[2], a0.x, a0.y, c0r, c0i, hi);
;         scan16(acc[1], acc[3], a1.x, a1.y, c1r, c1i, hi);
.LBB0_654:
	s_waitcnt vmcnt(2)
	v_cndmask_b32_e64 v19, v85, v81, s[8:9]
	v_cndmask_b32_e64 v18, v84, v80, s[8:9]
	v_cndmask_b32_e64 v17, v83, v79, s[8:9]
	v_cndmask_b32_e64 v16, v82, v78, s[8:9]
	v_cndmask_b32_e64 v0, 0, v0, s[36:37]
	v_cndmask_b32_e64 v1, 0, v1, s[36:37]
	v_mfma_f32_32x32x16_bf16 v[46:61], v[16:19], v[70:73], 0
	v_mul_f32_e32 v3, v113, v0
	v_mul_f32_e32 v2, v113, v1
	v_fmac_f32_e32 v3, v112, v1
	v_fma_f32 v0, v112, v0, -v2
	s_nop 7
	v_add_f32_e32 v132, v3, v46
	v_mfma_f32_32x32x16_bf16 v[30:45], v[16:19], v[62:65], 0
	s_nop 11
	v_add_f32_e32 v130, v30, v0
	v_pk_mul_f32 v[0:1], v[118:119], v[132:133] op_sel_hi:[1,0]
	v_mov_b32_e32 v46, v31
	v_pk_fma_f32 v[2:3], v[112:113], v[130:131], v[0:1] neg_lo:[0,0,1] neg_hi:[0,0,1]
	v_pk_fma_f32 v[0:1], v[112:113], v[130:131], v[0:1] op_sel_hi:[1,0,1]
	s_nop 0
	v_mov_b32_e32 v3, v1
	v_pk_add_f32 v[46:47], v[46:47], v[2:3]
	s_nop 0
	v_pk_mul_f32 v[0:1], v[112:113], v[46:47]
	s_nop 0
	v_sub_f32_e32 v20, v0, v1
	v_add_f32_e32 v32, v32, v20
	v_pk_mul_f32 v[20:21], v[118:119], v[46:47]
	v_mfma_f32_32x32x16_bf16 v[0:15], v[16:19], v[66:69], 0
	v_add_f32_e32 v20, v20, v21
	v_add_f32_e32 v134, v48, v20
	v_mul_f32_e64 v20, v118, v134
	v_mul_f32_e64 v21, v119, v134
	v_mov_b32_e32 v48, v33
	v_pk_fma_f32 v[136:137], v[112:113], v[32:33], v[20:21] neg_lo:[0,0,1] neg_hi:[0,0,1]
	v_pk_fma_f32 v[138:139], v[112:113], v[32:33], v[20:21] op_sel_hi:[1,0,1]
	s_nop 0
	v_mov_b32_e32 v137, v139
	v_pk_add_f32 v[48:49], v[48:49], v[136:137]
	v_mfma_f32_32x32x16_bf16 v[16:31], v[16:19], v[74:77], 0
	v_mul_f32_e64 v136, v112, v48
	v_mul_f32_e64 v137, v113, v49
	v_sub_f32_e32 v33, v136, v137
	v_mul_f32_e64 v136, v118, v48
	v_mul_f32_e64 v137, v119, v49
	v_add_f32_e32 v34, v34, v33
	v_add_f32_e32 v33, v136, v137
	v_add_f32_e32 v136, v50, v33
	v_pk_mul_f32 v[138:139], v[118:119], v[136:137] op_sel_hi:[1,0]
	v_mov_b32_e32 v50, v35
	v_pk_fma_f32 v[140:141], v[112:113], v[34:35], v[138:139] neg_lo:[0,0,1] neg_hi:[0,0,1]
	v_pk_fma_f32 v[138:139], v[112:113], v[34:35], v[138:139] op_sel_hi:[1,0,1]
	s_nop 0
	v_mov_b32_e32 v141, v139
	v_pk_add_f32 v[138:139], v[50:51], v[140:141]
	s_nop 0
	v_pk_mul_f32 v[50:51], v[112:113], v[138:139]
	s_nop 0
	v_sub_f32_e32 v33, v50, v51
	v_pk_mul_f32 v[50:51], v[118:119], v[138:139]
	v_add_f32_e32 v140, v36, v33
	v_add_f32_e32 v33, v50, v51
	v_add_f32_e32 v142, v52, v33
	v_pk_mul_f32 v[50:51], v[118:119], v[142:143] op_sel_hi:[1,0]
	v_mov_b32_e32 v52, v37
	v_pk_fma_f32 v[144:145], v[112:113], v[140:141], v[50:51] neg_lo:[0,0,1] neg_hi:[0,0,1]
	v_pk_fma_f32 v[50:51], v[112:113], v[140:141], v[50:51] op_sel_hi:[1,0,1]
	s_nop 0
	v_mov_b32_e32 v145, v51
	v_pk_add_f32 v[144:145], v[52:53], v[144:145]
	s_nop 0
	v_pk_mul_f32 v[36:37], v[112:113], v[144:145]
	s_nop 0
	v_sub_f32_e32 v33, v36, v37
	v_pk_mul_f32 v[36:37], v[118:119], v[144:145]
	v_add_f32_e32 v146, v38, v33
	v_add_f32_e32 v33, v36, v37
	v_add_f32_e32 v148, v54, v33
	v_pk_mul_f32 v[36:37], v[118:119], v[148:149] op_sel_hi:[1,0]
	v_mov_b32_e32 v54, v39
	v_pk_fma_f32 v[50:51], v[112:113], v[146:147], v[36:37] neg_lo:[0,0,1] neg_hi:[0,0,1]
	v_pk_fma_f32 v[36:37], v[112:113], v[146:147], v[36:37] op_sel_hi:[1,0,1]
	s_nop 0
	v_mov_b32_e32 v51, v37
	v_pk_add_f32 v[54:55], v[54:55], v[50:51]
	s_nop 0
	v_pk_mul_f32 v[36:37], v[112:113], v[54:55]
	s_nop 0
	v_sub_f32_e32 v33, v36, v37
	v_pk_mul_f32 v[36:37], v[118:119], v[54:55]
	v_add_f32_e32 v150, v40, v33
	v_add_f32_e32 v33, v36, v37
	v_add_f32_e32 v152, v56, v33
	v_pk_mul_f32 v[36:37], v[118:119], v[152:153] op_sel_hi:[1,0]
	v_mov_b32_e32 v56, v41
	v_pk_fma_f32 v[38:39], v[112:113], v[150:151], v[36:37] neg_lo:[0,0,1] neg_hi:[0,0,1]
	v_pk_fma_f32 v[36:37], v[112:113], v[150:151], v[36:37] op_sel_hi:[1,0,1]
	s_nop 0
	v_mov_b32_e32 v39, v37
	v_pk_add_f32 v[56:57], v[56:57], v[38:39]
	s_nop 0
	v_pk_mul_f32 v[36:37], v[112:113], v[56:57]
	s_nop 0
	v_sub_f32_e32 v33, v36, v37
	v_pk_mul_f32 v[36:37], v[118:119], v[56:57]
	v_add_f32_e32 v154, v42, v33
	v_add_f32_e32 v33, v36, v37
	v_add_f32_e32 v156, v58, v33
	v_pk_mul_f32 v[36:37], v[118:119], v[156:157] op_sel_hi:[1,0]
	v_mov_b32_e32 v58, v43
	v_pk_fma_f32 v[38:39], v[112:113], v[154:155], v[36:37] neg_lo:[0,0,1] neg_hi:[0,0,1]
	v_pk_fma_f32 v[36:37], v[112:113], v[154:155], v[36:37] op_sel_hi:[1,0,1]
	s_nop 0
	v_mov_b32_e32 v39, v37
	v_pk_add_f32 v[58:59], v[58:59], v[38:39]
	s_nop 0
	v_pk_mul_f32 v[36:37], v[112:113], v[58:59]
	s_nop 0
	v_sub_f32_e32 v33, v36, v37
	v_pk_mul_f32 v[36:37], v[118:119], v[58:59]
	v_add_f32_e32 v158, v44, v33
	v_add_f32_e32 v33, v36, v37
	v_add_f32_e32 v160, v60, v33
	v_pk_mul_f32 v[36:37], v[118:119], v[160:161] op_sel_hi:[1,0]
	v_mov_b32_e32 v60, v45
	v_pk_fma_f32 v[38:39], v[112:113], v[158:159], v[36:37] neg_lo:[0,0,1] neg_hi:[0,0,1]
	v_pk_fma_f32 v[36:37], v[112:113], v[158:159], v[36:37] op_sel_hi:[1,0,1]
	s_nop 0
	v_mov_b32_e32 v39, v37
	v_pk_add_f32 v[60:61], v[60:61], v[38:39]
	v_mov_b32_e32 v39, v113
	v_mov_b32_e32 v33, v60
	v_mov_b32_e32 v35, v60
	s_nop 1
	v_permlane32_swap_b32 v33, v35
	v_mov_b32_e32 v36, v61
	v_mov_b32_e32 v35, v61
	s_nop 1
	v_permlane32_swap_b32 v36, v35
	v_mov_b32_e32 v38, v112
	v_cndmask_b32_e64 v163, v36, 0, s[36:37]
	v_cndmask_b32_e64 v162, v33, 0, s[36:37]
	s_nop 0
	v_mul_f32_e32 v33, v163, v39
	v_fma_f32 v33, v162, v38, -v33
	v_add_f32_e32 v42, v130, v33
	v_mul_f32_e32 v33, v162, v39
	v_mul_f32_e32 v40, v113, v39
	v_fmac_f32_e32 v33, v163, v38
	v_pk_fma_f32 v[40:41], v[112:113], v[38:39], v[40:41] op_sel_hi:[1,1,0] neg_lo:[0,0,1] neg_hi:[0,0,1]
	v_mov_b32_e32 v44, v39
	v_mov_b32_e32 v45, v38
	v_mul_f32_e32 v38, v113, v38
	v_add_f32_e32 v36, v132, v33
; __device__ __forceinline__ float partner32(float v, int hi) { float r0, r1; swap32(v, r0, r1); return hi ? r0 : r1; }
; __device__ __forceinline__ void scan16(f32x16& re, f32x16& im, float ar, float ai, float& cr, float& ci, int hi) {
;     ...
;     float xr = partner32(sr, hi), xi = partner32(si, hi);
;     xr = hi ? xr : 0.f; xi = hi ? xi : 0.f;
;     float pr = ar, pi = ai; asm volatile("" : "+v"(pr), "+v"(pi));
; #pragma unroll
;     for (int r = 0; r < 16; ++r) { re[r] += pr * xr - pi * xi; im[r] += pr * xi + pi * xr; const float t = pr * ar - pi * ai; pi = pr * ai + pi * ar; pr = t; }
;     const float er = partner32(re[15], hi), ei = partner32(im[15], hi);
;     cr = hi ? re[15] : er; ci = hi ? im[15] : ei;
; }
	v_pk_fma_f32 v[38:39], v[112:113], v[44:45], v[38:39] op_sel_hi:[1,1,0]
	v_mul_f32_e32 v33, v162, v40
	v_fma_f32 v33, -v163, v38, v33
	v_add_f32_e32 v44, v46, v33
	v_mul_f32_e32 v33, v163, v40
	v_fmac_f32_e32 v33, v162, v38
	v_pk_mul_f32 v[38:39], v[112:113], v[38:39] op_sel_hi:[1,0]
	v_add_f32_e32 v37, v47, v33
	v_pk_fma_f32 v[46:47], v[118:119], v[40:41], v[38:39] op_sel_hi:[1,0,1] neg_lo:[0,0,1] neg_hi:[0,0,1]
	v_pk_fma_f32 v[40:41], v[118:119], v[40:41], v[38:39] op_sel_hi:[1,0,1]
	v_mul_f32_e32 v33, v162, v47
	v_mov_b32_e32 v50, v40
	v_mov_b32_e32 v51, v47
	v_fma_f32 v33, -v163, v40, v33
	v_pk_mov_b32 v[52:53], v[46:47], v[40:41] op_sel:[1,0]
	v_add_f32_e32 v46, v32, v33
	v_pk_mul_f32 v[32:33], v[162:163], v[50:51]
	s_nop 0
	v_add_f32_e32 v32, v33, v32
	v_add_f32_e32 v38, v134, v32
	v_mul_f32_e32 v32, v113, v40
	v_pk_fma_f32 v[32:33], v[112:113], v[52:53], v[32:33] op_sel_hi:[1,1,0] neg_lo:[0,0,1] neg_hi:[0,0,1]
	v_mul_f32_e32 v40, v113, v47
	v_pk_fma_f32 v[40:41], v[112:113], v[50:51], v[40:41] op_sel_hi:[1,1,0]
	v_mul_f32_e32 v35, v162, v32
	v_fma_f32 v35, -v163, v40, v35
	v_add_f32_e32 v48, v48, v35
	v_mul_f32_e32 v35, v163, v32
	v_fmac_f32_e32 v35, v162, v40
	v_pk_mul_f32 v[40:41], v[118:119], v[40:41] op_sel_hi:[1,0]
	v_add_f32_e32 v39, v49, v35
	v_pk_fma_f32 v[52:53], v[112:113], v[32:33], v[40:41] op_sel_hi:[1,0,1] neg_lo:[0,0,1] neg_hi:[0,0,1]
	v_pk_fma_f32 v[32:33], v[112:113], v[32:33], v[40:41] op_sel_hi:[1,0,1]
	s_nop 0
	v_mov_b32_e32 v53, v33
	v_pk_mul_f32 v[40:41], v[162:163], v[52:53]
	s_nop 0
	v_sub_f32_e32 v32, v40, v41
	v_add_f32_e32 v50, v34, v32
	v_mul_f32_e32 v32, v163, v52
	v_fmac_f32_e32 v32, v162, v33
	v_add_f32_e32 v40, v136, v32
	v_mul_f32_e32 v32, v113, v33
	v_pk_fma_f32 v[34:35], v[112:113], v[52:53], v[32:33] op_sel_hi:[1,1,0] neg_lo:[0,0,1] neg_hi:[0,0,1]
	v_mul_f32_e32 v32, v119, v33
	v_pk_fma_f32 v[32:33], v[118:119], v[52:53], v[32:33] op_sel_hi:[1,1,0]
	v_mul_f32_e32 v41, v162, v34
	v_fma_f32 v41, -v163, v32, v41
	v_add_f32_e32 v52, v41, v138
	v_mul_f32_e32 v41, v163, v34
	v_fmac_f32_e32 v41, v162, v32
	v_pk_mul_f32 v[32:33], v[118:119], v[32:33] op_sel_hi:[1,0]
	v_add_f32_e32 v41, v41, v139
	v_pk_fma_f32 v[130:131], v[112:113], v[34:35], v[32:33] op_sel_hi:[1,0,1] neg_lo:[0,0,1] neg_hi:[0,0,1]
	v_pk_fma_f32 v[32:33], v[112:113], v[34:35], v[32:33] op_sel_hi:[1,0,1]
	s_nop 0
	v_mov_b32_e32 v131, v33
	v_pk_mul_f32 v[34:35], v[162:163], v[130:131]
	s_nop 0
	v_sub_f32_e32 v32, v34, v35
	v_add_f32_e32 v140, v32, v140
	v_mul_f32_e32 v32, v163, v130
	v_fmac_f32_e32 v32, v162, v33
	v_add_f32_e32 v43, v32, v142
	v_mul_f32_e32 v32, v113, v33
	v_pk_fma_f32 v[34:35], v[112:113], v[130:131], v[32:33] op_sel_hi:[1,1,0] neg_lo:[0,0,1] neg_hi:[0,0,1]
	v_mul_f32_e32 v32, v119, v33
	v_pk_fma_f32 v[32:33], v[118:119], v[130:131], v[32:33] op_sel_hi:[1,1,0]
	v_mul_f32_e32 v45, v162, v34
	v_fma_f32 v45, -v163, v32, v45
	v_add_f32_e32 v141, v45, v144
	v_mul_f32_e32 v45, v163, v34
	v_fmac_f32_e32 v45, v162, v32
	v_pk_mul_f32 v[32:33], v[112:113], v[32:33] op_sel_hi:[1,0]
	v_add_f32_e32 v45, v45, v145
	v_pk_fma_f32 v[130:131], v[118:119], v[34:35], v[32:33] op_sel_hi:[1,0,1] neg_lo:[0,0,1] neg_hi:[0,0,1]
	v_pk_fma_f32 v[32:33], v[118:119], v[34:35], v[32:33] op_sel_hi:[1,0,1]
	v_mov_b32_e32 v35, v131
	v_mov_b32_e32 v34, v32
	v_pk_mov_b32 v[132:133], v[130:131], v[32:33] op_sel:[1,0]
	v_mul_f32_e32 v33, v162, v131
	v_fma_f32 v33, -v163, v32, v33
	v_pk_mul_f32 v[134:135], v[162:163], v[34:35]
	v_add_f32_e32 v142, v33, v146
	v_add_f32_e32 v33, v135, v134
	v_mul_f32_e32 v32, v113, v32
	v_add_f32_e32 v47, v33, v148
	v_pk_fma_f32 v[32:33], v[112:113], v[132:133], v[32:33] op_sel_hi:[1,1,0] neg_lo:[0,0,1] neg_hi:[0,0,1]
	v_mul_f32_e32 v130, v113, v131
	v_pk_fma_f32 v[34:35], v[112:113], v[34:35], v[130:131] op_sel_hi:[1,1,0]
	v_mul_f32_e32 v49, v162, v32
	v_fma_f32 v49, -v163, v34, v49
	v_add_f32_e32 v143, v49, v54
	v_mul_f32_e32 v49, v163, v32
	v_fmac_f32_e32 v49, v162, v34
	v_pk_mul_f32 v[34:35], v[118:119], v[34:35] op_sel_hi:[1,0]
	v_add_f32_e32 v49, v49, v55
	v_pk_fma_f32 v[54:55], v[112:113], v[32:33], v[34:35] op_sel_hi:[1,0,1] neg_lo:[0,0,1] neg_hi:[0,0,1]
	v_pk_fma_f32 v[32:33], v[112:113], v[32:33], v[34:35] op_sel_hi:[1,0,1]
	s_nop 0
	v_mov_b32_e32 v55, v33
	v_pk_mul_f32 v[34:35], v[162:163], v[54:55]
	s_nop 0
	v_sub_f32_e32 v32, v34, v35
	v_add_f32_e32 v144, v32, v150
	v_mul_f32_e32 v32, v163, v54
	v_fmac_f32_e32 v32, v162, v33
	v_add_f32_e32 v51, v32, v152
	v_mul_f32_e32 v32, v113, v33
	v_pk_fma_f32 v[34:35], v[112:113], v[54:55], v[32:33] op_sel_hi:[1,1,0] neg_lo:[0,0,1] neg_hi:[0,0,1]
	v_mul_f32_e32 v32, v119, v33
	v_pk_fma_f32 v[32:33], v[118:119], v[54:55], v[32:33] op_sel_hi:[1,1,0]
	v_mul_f32_e32 v53, v162, v34
	v_fma_f32 v53, -v163, v32, v53
	v_add_f32_e32 v145, v53, v56
	v_mul_f32_e32 v53, v163, v34
	v_fmac_f32_e32 v53, v162, v32
	v_pk_mul_f32 v[32:33], v[118:119], v[32:33] op_sel_hi:[1,0]
	v_add_f32_e32 v53, v53, v57
	v_pk_fma_f32 v[54:55], v[112:113], v[34:35], v[32:33] op_sel_hi:[1,0,1] neg_lo:[0,0,1] neg_hi:[0,0,1]
	v_pk_fma_f32 v[32:33], v[112:113], v[34:35], v[32:33] op_sel_hi:[1,0,1]
	s_nop 0
	v_mov_b32_e32 v55, v33
	v_pk_mul_f32 v[34:35], v[162:163], v[54:55]
	s_nop 0
	v_sub_f32_e32 v32, v34, v35
	v_add_f32_e32 v146, v32, v154
	v_mul_f32_e32 v32, v163, v54
	v_fmac_f32_e32 v32, v162, v33
	v_add_f32_e32 v147, v32, v156
	v_mul_f32_e32 v32, v113, v33
	v_pk_fma_f32 v[34:35], v[112:113], v[54:55], v[32:33] op_sel_hi:[1,1,0] neg_lo:[0,0,1] neg_hi:[0,0,1]
	v_mul_f32_e32 v32, v119, v33
	v_pk_fma_f32 v[32:33], v[118:119], v[54:55], v[32:33] op_sel_hi:[1,1,0]
	v_mul_f32_e32 v54, v162, v34
	v_fma_f32 v54, -v163, v32, v54
; __device__ __forceinline__ float partner32(float v, int hi) { float r0, r1; swap32(v, r0, r1); return hi ? r0 : r1; }
; __device__ __forceinline__ void scan16(f32x16& re, f32x16& im, float ar, float ai, float& cr, float& ci, int hi) {
;     float sr = hi ? 0.f : cr, si = hi ? 0.f : ci;
; #pragma unroll
;     for (int r = 0; r < 16; ++r) { const float nr = ar * sr - ai * si + re[r], ni = ar * si + ai * sr + im[r]; sr = nr; si = ni; re[r] = sr; im[r] = si; }
;     float xr = partner32(sr, hi), xi = partner32(si, hi);
;     xr = hi ? xr : 0.f; xi = hi ? xi : 0.f;
;     float pr = ar, pi = ai; asm volatile("" : "+v"(pr), "+v"(pi));
; #pragma unroll
;     for (int r = 0; r < 16; ++r) { re[r] += pr * xr - pi * xi; im[r] += pr * xi + pi * xr; const float t = pr * ar - pi * ai; pi = pr * ai + pi * ar; pr = t; }
;     const float er = partner32(re[15], hi), ei = partner32(im[15], hi);
;     cr = hi ? re[15] : er; ci = hi ? im[15] : ei;
; }
	v_add_f32_e32 v148, v54, v58
	v_mul_f32_e32 v54, v163, v34
	v_fmac_f32_e32 v54, v162, v32
	v_pk_mul_f32 v[32:33], v[112:113], v[32:33] op_sel_hi:[1,0]
	v_add_f32_e32 v149, v54, v59
	v_pk_fma_f32 v[54:55], v[118:119], v[34:35], v[32:33] op_sel_hi:[1,0,1] neg_lo:[0,0,1] neg_hi:[0,0,1]
	v_pk_fma_f32 v[32:33], v[118:119], v[34:35], v[32:33] op_sel_hi:[1,0,1]
	v_mov_b32_e32 v35, v55
	v_pk_mov_b32 v[56:57], v[54:55], v[32:33] op_sel:[1,0]
	v_mul_f32_e32 v33, v162, v55
	v_mov_b32_e32 v34, v32
	v_fma_f32 v32, -v163, v32, v33
	v_add_f32_e32 v150, v32, v158
	v_pk_mul_f32 v[32:33], v[162:163], v[34:35]
	v_pk_mul_f32 v[34:35], v[112:113], v[34:35]
	v_add_f32_e32 v32, v33, v32
	v_add_f32_e32 v151, v32, v160
	v_pk_mul_f32 v[32:33], v[112:113], v[56:57]
	v_pk_add_f32 v[34:35], v[34:35], v[34:35] op_sel:[1,0] op_sel_hi:[1,0]
	v_pk_add_f32 v[32:33], v[32:33], v[32:33] op_sel:[0,1] op_sel_hi:[0,1] neg_lo:[0,1] neg_hi:[0,1]
	v_pk_mul_f32 v[34:35], v[162:163], v[34:35] op_sel:[1,0] op_sel_hi:[0,1]
	v_pk_fma_f32 v[54:55], v[162:163], v[32:33], v[34:35] neg_lo:[0,0,1] neg_hi:[0,0,1]
	v_pk_fma_f32 v[32:33], v[162:163], v[32:33], v[34:35]
	s_nop 0
	v_mov_b32_e32 v55, v33
	v_pk_add_f32 v[32:33], v[54:55], v[60:61]
	v_cndmask_b32_e64 v55, 0, v123, s[36:37]
	v_mov_b32_e32 v35, v32
	v_mov_b32_e32 v34, v32
	s_nop 1
	v_permlane32_swap_b32 v35, v34
	v_mov_b32_e32 v54, v33
	v_mov_b32_e32 v35, v33
	s_nop 1
	v_permlane32_swap_b32 v54, v35
	v_mul_f32_e32 v56, v115, v55
	v_cndmask_b32_e64 v54, 0, v122, s[36:37]
	v_fma_f32 v56, v114, v54, -v56
	v_mul_f32_e32 v54, v115, v54
	v_fmac_f32_e32 v54, v114, v55
	v_add_f32_e32 v54, v54, v16
	v_add_f32_e32 v0, v56, v0
	v_pk_mul_f32 v[56:57], v[120:121], v[54:55] op_sel_hi:[1,0]
	v_mov_b32_e32 v16, v1
	v_pk_fma_f32 v[58:59], v[114:115], v[0:1], v[56:57] neg_lo:[0,0,1] neg_hi:[0,0,1]
	v_pk_fma_f32 v[56:57], v[114:115], v[0:1], v[56:57] op_sel_hi:[1,0,1]
	s_nop 0
	v_mov_b32_e32 v59, v57
	v_pk_add_f32 v[16:17], v[16:17], v[58:59]
	s_nop 0
	v_pk_mul_f32 v[56:57], v[114:115], v[16:17]
	s_nop 0
	v_sub_f32_e32 v1, v56, v57
	v_pk_mul_f32 v[56:57], v[120:121], v[16:17]
	v_add_f32_e32 v2, v2, v1
	v_add_f32_e32 v1, v56, v57
	v_add_f32_e32 v56, v18, v1
	v_pk_mul_f32 v[58:59], v[120:121], v[56:57] op_sel_hi:[1,0]
	v_mov_b32_e32 v18, v3
	v_pk_fma_f32 v[60:61], v[114:115], v[2:3], v[58:59] neg_lo:[0,0,1] neg_hi:[0,0,1]
	v_pk_fma_f32 v[58:59], v[114:115], v[2:3], v[58:59] op_sel_hi:[1,0,1]
	s_nop 0
	v_mov_b32_e32 v61, v59
	v_pk_add_f32 v[18:19], v[18:19], v[60:61]
	s_nop 0
	v_pk_mul_f32 v[58:59], v[114:115], v[18:19]
	s_nop 0
	v_sub_f32_e32 v1, v58, v59
	v_pk_mul_f32 v[58:59], v[120:121], v[18:19]
	v_add_f32_e32 v4, v4, v1
	v_add_f32_e32 v1, v58, v59
	v_add_f32_e32 v58, v20, v1
	v_pk_mul_f32 v[60:61], v[120:121], v[58:59] op_sel_hi:[1,0]
	v_mov_b32_e32 v20, v5
	v_pk_fma_f32 v[122:123], v[114:115], v[4:5], v[60:61] neg_lo:[0,0,1] neg_hi:[0,0,1]
	v_pk_fma_f32 v[60:61], v[114:115], v[4:5], v[60:61] op_sel_hi:[1,0,1]
	s_nop 0
	v_mov_b32_e32 v123, v61
	v_pk_add_f32 v[20:21], v[20:21], v[122:123]
	s_nop 0
	v_pk_mul_f32 v[60:61], v[114:115], v[20:21]
	s_nop 0
	v_sub_f32_e32 v1, v60, v61
	v_pk_mul_f32 v[60:61], v[120:121], v[20:21]
	v_add_f32_e32 v6, v6, v1
	v_add_f32_e32 v1, v60, v61
	v_add_f32_e32 v60, v22, v1
	v_pk_mul_f32 v[122:123], v[120:121], v[60:61] op_sel_hi:[1,0]
	v_mov_b32_e32 v22, v7
	v_pk_fma_f32 v[130:131], v[114:115], v[6:7], v[122:123] neg_lo:[0,0,1] neg_hi:[0,0,1]
	v_pk_fma_f32 v[122:123], v[114:115], v[6:7], v[122:123] op_sel_hi:[1,0,1]
	s_nop 0
	v_mov_b32_e32 v131, v123
	v_pk_add_f32 v[22:23], v[22:23], v[130:131]
	s_nop 0
	v_pk_mul_f32 v[122:123], v[114:115], v[22:23]
	s_nop 0
	v_sub_f32_e32 v1, v122, v123
	v_pk_mul_f32 v[122:123], v[120:121], v[22:23]
	v_add_f32_e32 v8, v8, v1
	v_add_f32_e32 v1, v122, v123
	v_add_f32_e32 v122, v24, v1
	v_pk_mul_f32 v[130:131], v[120:121], v[122:123] op_sel_hi:[1,0]
	v_mov_b32_e32 v24, v9
	v_pk_fma_f32 v[132:133], v[114:115], v[8:9], v[130:131] neg_lo:[0,0,1] neg_hi:[0,0,1]
	v_pk_fma_f32 v[130:131], v[114:115], v[8:9], v[130:131] op_sel_hi:[1,0,1]
	s_nop 0
	v_mov_b32_e32 v133, v131
	v_pk_add_f32 v[24:25], v[24:25], v[132:133]
	s_nop 0
	v_pk_mul_f32 v[130:131], v[114:115], v[24:25]
	s_nop 0
	v_sub_f32_e32 v1, v130, v131
	v_pk_mul_f32 v[130:131], v[120:121], v[24:25]
	v_add_f32_e32 v10, v10, v1
	v_add_f32_e32 v1, v130, v131
	v_add_f32_e32 v130, v26, v1
	v_pk_mul_f32 v[132:133], v[120:121], v[130:131] op_sel_hi:[1,0]
	v_mov_b32_e32 v26, v11
	v_pk_fma_f32 v[134:135], v[114:115], v[10:11], v[132:133] neg_lo:[0,0,1] neg_hi:[0,0,1]
	v_pk_fma_f32 v[132:133], v[114:115], v[10:11], v[132:133] op_sel_hi:[1,0,1]
	s_nop 0
	v_mov_b32_e32 v135, v133
	v_pk_add_f32 v[26:27], v[26:27], v[134:135]
	s_nop 0
	v_pk_mul_f32 v[132:133], v[114:115], v[26:27]
	s_nop 0
	v_sub_f32_e32 v1, v132, v133
	v_pk_mul_f32 v[132:133], v[120:121], v[26:27]
	v_add_f32_e32 v12, v12, v1
	v_add_f32_e32 v1, v132, v133
	v_add_f32_e32 v132, v28, v1
	v_pk_mul_f32 v[134:135], v[120:121], v[132:133] op_sel_hi:[1,0]
	v_mov_b32_e32 v28, v13
	v_pk_fma_f32 v[136:137], v[114:115], v[12:13], v[134:135] neg_lo:[0,0,1] neg_hi:[0,0,1]
	v_pk_fma_f32 v[134:135], v[114:115], v[12:13], v[134:135] op_sel_hi:[1,0,1]
	s_nop 0
	v_mov_b32_e32 v137, v135
	v_pk_add_f32 v[28:29], v[28:29], v[136:137]
	s_nop 0
	v_pk_mul_f32 v[134:135], v[114:115], v[28:29]
	s_nop 0
	v_sub_f32_e32 v1, v134, v135
	v_pk_mul_f32 v[134:135], v[120:121], v[28:29]
	v_add_f32_e32 v14, v14, v1
	v_add_f32_e32 v1, v134, v135
	v_add_f32_e32 v134, v30, v1
	v_pk_mul_f32 v[136:137], v[120:121], v[134:135] op_sel_hi:[1,0]
	v_mov_b32_e32 v30, v15
	v_pk_fma_f32 v[138:139], v[114:115], v[14:15], v[136:137] neg_lo:[0,0,1] neg_hi:[0,0,1]
; __device__ __forceinline__ float partner32(float v, int hi) { float r0, r1; swap32(v, r0, r1); return hi ? r0 : r1; }
; __device__ __forceinline__ void scan16(f32x16& re, f32x16& im, float ar, float ai, float& cr, float& ci, int hi) {
;     ...
;     float xr = partner32(sr, hi), xi = partner32(si, hi);
;     xr = hi ? xr : 0.f; xi = hi ? xi : 0.f;
;     float pr = ar, pi = ai; asm volatile("" : "+v"(pr), "+v"(pi));
; #pragma unroll
;     for (int r = 0; r < 16; ++r) { re[r] += pr * xr - pi * xi; im[r] += pr * xi + pi * xr; const float t = pr * ar - pi * ai; pi = pr * ai + pi * ar; pr = t; }
;     const float er = partner32(re[15], hi), ei = partner32(im[15], hi);
;     cr = hi ? re[15] : er; ci = hi ? im[15] : ei;
; }
	v_pk_fma_f32 v[136:137], v[114:115], v[14:15], v[136:137] op_sel_hi:[1,0,1]
	s_nop 0
	v_mov_b32_e32 v139, v137
	v_pk_add_f32 v[30:31], v[30:31], v[138:139]
	v_mov_b32_e32 v139, v115
	v_mov_b32_e32 v1, v30
	v_mov_b32_e32 v3, v30
	s_nop 1
	v_permlane32_swap_b32 v3, v1
	v_mov_b32_e32 v5, v31
	v_mov_b32_e32 v1, v31
	s_nop 1
	v_permlane32_swap_b32 v1, v5
	v_mov_b32_e32 v138, v114
	v_cndmask_b32_e64 v137, v1, 0, s[36:37]
	v_cndmask_b32_e64 v136, v3, 0, s[36:37]
	s_nop 0
	v_mul_f32_e32 v1, v137, v139
	v_fma_f32 v1, v136, v138, -v1
	v_add_f32_e32 v11, v0, v1
	v_mul_f32_e32 v0, v136, v139
	v_fmac_f32_e32 v0, v137, v138
	v_add_f32_e32 v13, v54, v0
	v_mul_f32_e32 v0, v115, v139
	v_pk_fma_f32 v[0:1], v[114:115], v[138:139], v[0:1] op_sel_hi:[1,1,0] neg_lo:[0,0,1] neg_hi:[0,0,1]
	v_mov_b32_e32 v54, v139
	v_mov_b32_e32 v55, v138
	v_mul_f32_e32 v138, v115, v138
	v_pk_fma_f32 v[54:55], v[114:115], v[54:55], v[138:139] op_sel_hi:[1,1,0]
	v_mul_f32_e32 v3, v136, v0
	v_fma_f32 v3, -v137, v54, v3
	v_add_f32_e32 v15, v16, v3
	v_mul_f32_e32 v3, v137, v0
	v_fmac_f32_e32 v3, v136, v54
	v_add_f32_e32 v57, v17, v3
	v_pk_mul_f32 v[16:17], v[114:115], v[54:55] op_sel_hi:[1,0]
	s_nop 0
	v_pk_fma_f32 v[54:55], v[120:121], v[0:1], v[16:17] op_sel_hi:[1,0,1] neg_lo:[0,0,1] neg_hi:[0,0,1]
	v_pk_fma_f32 v[0:1], v[120:121], v[0:1], v[16:17] op_sel_hi:[1,0,1]
	v_mov_b32_e32 v17, v55
	v_pk_mov_b32 v[138:139], v[54:55], v[0:1] op_sel:[1,0]
	v_mul_f32_e32 v1, v136, v55
	v_mov_b32_e32 v16, v0
	v_fma_f32 v1, -v137, v0, v1
	v_add_f32_e32 v54, v2, v1
	v_pk_mul_f32 v[2:3], v[136:137], v[16:17]
	v_mul_f32_e32 v0, v115, v0
	v_add_f32_e32 v1, v3, v2
	v_add_f32_e32 v56, v56, v1
	v_pk_fma_f32 v[0:1], v[114:115], v[138:139], v[0:1] op_sel_hi:[1,1,0] neg_lo:[0,0,1] neg_hi:[0,0,1]
	v_mul_f32_e32 v2, v115, v55
	v_pk_fma_f32 v[2:3], v[114:115], v[16:17], v[2:3] op_sel_hi:[1,1,0]
	v_mul_f32_e32 v5, v136, v0
	v_fma_f32 v5, -v137, v2, v5
	v_add_f32_e32 v55, v18, v5
	v_mul_f32_e32 v5, v137, v0
	v_fmac_f32_e32 v5, v136, v2
	v_pk_mul_f32 v[2:3], v[120:121], v[2:3] op_sel_hi:[1,0]
	v_add_f32_e32 v59, v19, v5
	v_pk_fma_f32 v[16:17], v[114:115], v[0:1], v[2:3] op_sel_hi:[1,0,1] neg_lo:[0,0,1] neg_hi:[0,0,1]
	v_pk_fma_f32 v[0:1], v[114:115], v[0:1], v[2:3] op_sel_hi:[1,0,1]
	s_nop 0
	v_mov_b32_e32 v17, v1
	v_pk_mul_f32 v[2:3], v[136:137], v[16:17]
	s_nop 0
	v_sub_f32_e32 v0, v2, v3
	v_add_f32_e32 v61, v4, v0
	v_mul_f32_e32 v0, v137, v16
	v_fmac_f32_e32 v0, v136, v1
	v_add_f32_e32 v58, v58, v0
	v_mul_f32_e32 v0, v115, v1
	v_pk_fma_f32 v[2:3], v[114:115], v[16:17], v[0:1] op_sel_hi:[1,1,0] neg_lo:[0,0,1] neg_hi:[0,0,1]
	v_mul_f32_e32 v0, v121, v1
	v_pk_fma_f32 v[0:1], v[120:121], v[16:17], v[0:1] op_sel_hi:[1,1,0]
	v_mul_f32_e32 v4, v136, v2
	v_fma_f32 v4, -v137, v0, v4
	v_add_f32_e32 v20, v20, v4
	v_mul_f32_e32 v4, v137, v2
	v_fmac_f32_e32 v4, v136, v0
	v_pk_mul_f32 v[0:1], v[120:121], v[0:1] op_sel_hi:[1,0]
	v_add_f32_e32 v21, v21, v4
	v_pk_fma_f32 v[4:5], v[114:115], v[2:3], v[0:1] op_sel_hi:[1,0,1] neg_lo:[0,0,1] neg_hi:[0,0,1]
	v_pk_fma_f32 v[0:1], v[114:115], v[2:3], v[0:1] op_sel_hi:[1,0,1]
	s_nop 0
	v_mov_b32_e32 v5, v1
	v_pk_mul_f32 v[2:3], v[136:137], v[4:5]
	s_nop 0
	v_sub_f32_e32 v0, v2, v3
	v_add_f32_e32 v123, v6, v0
	v_mul_f32_e32 v0, v137, v4
	v_fmac_f32_e32 v0, v136, v1
	v_add_f32_e32 v60, v60, v0
	v_mul_f32_e32 v0, v115, v1
	v_pk_fma_f32 v[2:3], v[114:115], v[4:5], v[0:1] op_sel_hi:[1,1,0] neg_lo:[0,0,1] neg_hi:[0,0,1]
	v_mul_f32_e32 v0, v121, v1
	v_pk_fma_f32 v[0:1], v[120:121], v[4:5], v[0:1] op_sel_hi:[1,1,0]
	v_mul_f32_e32 v4, v136, v2
	v_fma_f32 v4, -v137, v0, v4
	v_add_f32_e32 v22, v22, v4
	v_mul_f32_e32 v4, v137, v2
	v_fmac_f32_e32 v4, v136, v0
	v_pk_mul_f32 v[0:1], v[114:115], v[0:1] op_sel_hi:[1,0]
	v_add_f32_e32 v23, v23, v4
	v_pk_fma_f32 v[4:5], v[120:121], v[2:3], v[0:1] op_sel_hi:[1,0,1] neg_lo:[0,0,1] neg_hi:[0,0,1]
	v_pk_fma_f32 v[0:1], v[120:121], v[2:3], v[0:1] op_sel_hi:[1,0,1]
	v_mov_b32_e32 v3, v5
	v_pk_mov_b32 v[6:7], v[4:5], v[0:1] op_sel:[1,0]
	v_mul_f32_e32 v1, v136, v5
	v_mov_b32_e32 v2, v0
	v_fma_f32 v1, -v137, v0, v1
	v_add_f32_e32 v131, v8, v1
	v_pk_mul_f32 v[8:9], v[136:137], v[2:3]
	v_mul_f32_e32 v0, v115, v0
	v_add_f32_e32 v1, v9, v8
	v_add_f32_e32 v8, v122, v1
	v_pk_fma_f32 v[0:1], v[114:115], v[6:7], v[0:1] op_sel_hi:[1,1,0] neg_lo:[0,0,1] neg_hi:[0,0,1]
	v_mul_f32_e32 v4, v115, v5
	v_pk_fma_f32 v[2:3], v[114:115], v[2:3], v[4:5] op_sel_hi:[1,1,0]
	v_mul_f32_e32 v4, v136, v0
	v_fma_f32 v4, -v137, v2, v4
	v_add_f32_e32 v9, v4, v24
	v_mul_f32_e32 v4, v137, v0
	v_fmac_f32_e32 v4, v136, v2
	v_pk_mul_f32 v[2:3], v[120:121], v[2:3] op_sel_hi:[1,0]
	v_add_f32_e32 v24, v4, v25
	v_pk_fma_f32 v[4:5], v[114:115], v[0:1], v[2:3] op_sel_hi:[1,0,1] neg_lo:[0,0,1] neg_hi:[0,0,1]
	v_pk_fma_f32 v[0:1], v[114:115], v[0:1], v[2:3] op_sel_hi:[1,0,1]
	s_nop 0
	v_mov_b32_e32 v5, v1
	v_pk_mul_f32 v[2:3], v[136:137], v[4:5]
	s_nop 0
	v_sub_f32_e32 v0, v2, v3
	v_add_f32_e32 v10, v0, v10
	v_mul_f32_e32 v0, v137, v4
	v_fmac_f32_e32 v0, v136, v1
	v_add_f32_e32 v25, v0, v130
	v_mul_f32_e32 v0, v115, v1
	v_pk_fma_f32 v[2:3], v[114:115], v[4:5], v[0:1] op_sel_hi:[1,1,0] neg_lo:[0,0,1] neg_hi:[0,0,1]
	v_mul_f32_e32 v0, v121, v1
	v_pk_fma_f32 v[0:1], v[120:121], v[4:5], v[0:1] op_sel_hi:[1,1,0]
	v_mul_f32_e32 v4, v136, v2
	v_fma_f32 v4, -v137, v0, v4
	v_add_f32_e32 v26, v4, v26
	v_mul_f32_e32 v4, v137, v2
	v_fmac_f32_e32 v4, v136, v0
	v_pk_mul_f32 v[0:1], v[120:121], v[0:1] op_sel_hi:[1,0]
	v_add_f32_e32 v27, v4, v27
	v_pk_fma_f32 v[4:5], v[114:115], v[2:3], v[0:1] op_sel_hi:[1,0,1] neg_lo:[0,0,1] neg_hi:[0,0,1]
	v_pk_fma_f32 v[0:1], v[114:115], v[2:3], v[0:1] op_sel_hi:[1,0,1]
; #define LAS __attribute__((address_space(3)))
; __device__ __forceinline__ unsigned f2bf(float f) { return hw_pk_bf16(f, 0.f) & 0xffffu; }
; __device__ __forceinline__ float partner32(float v, int hi) { float r0, r1; swap32(v, r0, r1); return hi ? r0 : r1; }
; __device__ __forceinline__ void scan16(f32x16& re, f32x16& im, float ar, float ai, float& cr, float& ci, int hi) {
;     ...
;     float xr = partner32(sr, hi), xi = partner32(si, hi);
;     xr = hi ? xr : 0.f; xi = hi ? xi : 0.f;
;     float pr = ar, pi = ai; asm volatile("" : "+v"(pr), "+v"(pi));
; #pragma unroll
;     for (int r = 0; r < 16; ++r) { re[r] += pr * xr - pi * xi; im[r] += pr * xi + pi * xr; const float t = pr * ar - pi * ai; pi = pr * ai + pi * ar; pr = t; }
;     const float er = partner32(re[15], hi), ei = partner32(im[15], hi);
;     cr = hi ? re[15] : er; ci = hi ? im[15] : ei;
; }
; template <bool FINAL>
; __device__ __forceinline__ void s5_group(int lane, const unsigned char* tab, const bf16* __restrict__ proj, f32x2* E, int c, int g, LAS bf16* sbuf, LAS bf16* yg) {
;     ...
;             LAS bf16* sw = sbuf + (16 * hi) * SB_PITCH + r32;
; #pragma unroll
;             for (int pt = 0; pt < 4; ++pt)
; #pragma unroll
;                 for (int r = 0; r < 16; ++r) sw[r * SB_PITCH + 32 * pt] = (bf16)f2bf(acc[pt][r]);
;             asm volatile("s_waitcnt lgkmcnt(0)" ::: "memory");
	s_nop 0
	v_mov_b32_e32 v5, v1
	v_pk_mul_f32 v[2:3], v[136:137], v[4:5]
	s_nop 0
	v_sub_f32_e32 v0, v2, v3
	v_add_f32_e32 v12, v0, v12
	v_mul_f32_e32 v0, v137, v4
	v_fmac_f32_e32 v0, v136, v1
	v_add_f32_e32 v122, v0, v132
	v_mul_f32_e32 v0, v115, v1
	v_pk_fma_f32 v[2:3], v[114:115], v[4:5], v[0:1] op_sel_hi:[1,1,0] neg_lo:[0,0,1] neg_hi:[0,0,1]
	v_mul_f32_e32 v0, v121, v1
	v_pk_fma_f32 v[0:1], v[120:121], v[4:5], v[0:1] op_sel_hi:[1,1,0]
	v_mul_f32_e32 v4, v136, v2
	v_fma_f32 v4, -v137, v0, v4
	v_add_f32_e32 v28, v4, v28
	v_mul_f32_e32 v4, v137, v2
	v_fmac_f32_e32 v4, v136, v0
	v_pk_mul_f32 v[0:1], v[114:115], v[0:1] op_sel_hi:[1,0]
	v_add_f32_e32 v29, v4, v29
	v_pk_fma_f32 v[4:5], v[120:121], v[2:3], v[0:1] op_sel_hi:[1,0,1] neg_lo:[0,0,1] neg_hi:[0,0,1]
	v_pk_fma_f32 v[0:1], v[120:121], v[2:3], v[0:1] op_sel_hi:[1,0,1]
	v_mov_b32_e32 v3, v5
	v_pk_mov_b32 v[6:7], v[4:5], v[0:1] op_sel:[1,0]
	v_mul_f32_e32 v1, v136, v5
	v_mov_b32_e32 v2, v0
	v_fma_f32 v0, -v137, v0, v1
	v_add_f32_e32 v14, v0, v14
	v_pk_mul_f32 v[0:1], v[136:137], v[2:3]
	v_pk_mul_f32 v[2:3], v[114:115], v[2:3]
	v_add_f32_e32 v0, v1, v0
	v_add_f32_e32 v130, v0, v134
	v_pk_mul_f32 v[0:1], v[114:115], v[6:7]
	v_pk_add_f32 v[2:3], v[2:3], v[2:3] op_sel:[1,0] op_sel_hi:[1,0]
	v_pk_add_f32 v[0:1], v[0:1], v[0:1] op_sel:[0,1] op_sel_hi:[0,1] neg_lo:[0,1] neg_hi:[0,1]
	v_pk_mul_f32 v[2:3], v[136:137], v[2:3] op_sel:[1,0] op_sel_hi:[0,1]
	v_pk_fma_f32 v[4:5], v[136:137], v[0:1], v[2:3] neg_lo:[0,0,1] neg_hi:[0,0,1]
	v_pk_fma_f32 v[0:1], v[136:137], v[0:1], v[2:3]
	s_nop 0
	v_mov_b32_e32 v5, v1
	v_pk_add_f32 v[16:17], v[4:5], v[30:31]
	s_nop 0
	v_mov_b32_e32 v18, v16
	v_mov_b32_e32 v0, v16
	s_nop 1
	v_permlane32_swap_b32 v0, v18
	v_mov_b32_e32 v19, v17
	v_mov_b32_e32 v0, v17
	s_nop 1
	v_permlane32_swap_b32 v0, v19
	s_nop 0
	v_cvt_pk_bf16_f32 v0, v42, s0
	ds_write_b16 v126, v0
	v_cvt_pk_bf16_f32 v0, v44, s0
	ds_write_b16 v126, v0 offset:272
	v_cvt_pk_bf16_f32 v0, v46, s0
	ds_write_b16 v126, v0 offset:544
	v_cvt_pk_bf16_f32 v0, v48, s0
	ds_write_b16 v126, v0 offset:816
	v_cvt_pk_bf16_f32 v0, v50, s0
	ds_write_b16 v126, v0 offset:1088
	v_cvt_pk_bf16_f32 v0, v52, s0
	ds_write_b16 v126, v0 offset:1360
	v_cvt_pk_bf16_f32 v0, v140, s0
	ds_write_b16 v126, v0 offset:1632
	v_cvt_pk_bf16_f32 v0, v141, s0
	ds_write_b16 v126, v0 offset:1904
	v_cvt_pk_bf16_f32 v0, v142, s0
	ds_write_b16 v126, v0 offset:2176
	v_cvt_pk_bf16_f32 v0, v143, s0
	ds_write_b16 v126, v0 offset:2448
	v_cvt_pk_bf16_f32 v0, v144, s0
	ds_write_b16 v126, v0 offset:2720
	v_cvt_pk_bf16_f32 v0, v145, s0
	ds_write_b16 v126, v0 offset:2992
	v_cvt_pk_bf16_f32 v0, v146, s0
	ds_write_b16 v126, v0 offset:3264
	v_cvt_pk_bf16_f32 v0, v148, s0
	ds_write_b16 v126, v0 offset:3536
	v_cvt_pk_bf16_f32 v0, v150, s0
	ds_write_b16 v126, v0 offset:3808
	v_cvt_pk_bf16_f32 v0, v32, s0
	ds_write_b16 v126, v0 offset:4080
	v_cvt_pk_bf16_f32 v0, v11, s0
	ds_write_b16 v126, v0 offset:64
	v_cvt_pk_bf16_f32 v0, v15, s0
	ds_write_b16 v126, v0 offset:336
	v_cvt_pk_bf16_f32 v0, v54, s0
	ds_write_b16 v126, v0 offset:608
	v_cvt_pk_bf16_f32 v0, v55, s0
	ds_write_b16 v126, v0 offset:880
	v_cvt_pk_bf16_f32 v0, v61, s0
	ds_write_b16 v126, v0 offset:1152
	v_cvt_pk_bf16_f32 v0, v20, s0
	ds_write_b16 v126, v0 offset:1424
	v_cvt_pk_bf16_f32 v0, v123, s0
	ds_write_b16 v126, v0 offset:1696
	v_cvt_pk_bf16_f32 v0, v22, s0
	ds_write_b16 v126, v0 offset:1968
	v_cvt_pk_bf16_f32 v0, v131, s0
	ds_write_b16 v126, v0 offset:2240
	v_cvt_pk_bf16_f32 v0, v9, s0
	ds_write_b16 v126, v0 offset:2512
	v_cvt_pk_bf16_f32 v0, v10, s0
	ds_write_b16 v126, v0 offset:2784
	v_cvt_pk_bf16_f32 v0, v26, s0
	ds_write_b16 v126, v0 offset:3056
	v_cvt_pk_bf16_f32 v0, v12, s0
	ds_write_b16 v126, v0 offset:3328
	v_cvt_pk_bf16_f32 v0, v28, s0
	ds_write_b16 v126, v0 offset:3600
	v_cvt_pk_bf16_f32 v0, v14, s0
	ds_write_b16 v126, v0 offset:3872
	v_cvt_pk_bf16_f32 v0, v16, s0
	ds_write_b16 v126, v0 offset:4144
	v_cvt_pk_bf16_f32 v0, v36, s0
	ds_write_b16 v126, v0 offset:128
	v_cvt_pk_bf16_f32 v0, v37, s0
	ds_write_b16 v126, v0 offset:400
	v_cvt_pk_bf16_f32 v0, v38, s0
	ds_write_b16 v126, v0 offset:672
	v_cvt_pk_bf16_f32 v0, v39, s0
	ds_write_b16 v126, v0 offset:944
	v_cvt_pk_bf16_f32 v0, v40, s0
	ds_write_b16 v126, v0 offset:1216
	v_cvt_pk_bf16_f32 v0, v41, s0
	ds_write_b16 v126, v0 offset:1488
	v_cvt_pk_bf16_f32 v0, v43, s0
	ds_write_b16 v126, v0 offset:1760
	v_cvt_pk_bf16_f32 v0, v45, s0
	ds_write_b16 v126, v0 offset:2032
	v_cvt_pk_bf16_f32 v0, v47, s0
	ds_write_b16 v126, v0 offset:2304
	v_cvt_pk_bf16_f32 v0, v49, s0
	ds_write_b16 v126, v0 offset:2576
	v_cvt_pk_bf16_f32 v0, v51, s0
	ds_write_b16 v126, v0 offset:2848
	v_cvt_pk_bf16_f32 v0, v53, s0
	ds_write_b16 v126, v0 offset:3120
	v_cvt_pk_bf16_f32 v0, v147, s0
	ds_write_b16 v126, v0 offset:3392
	v_cvt_pk_bf16_f32 v0, v149, s0
	ds_write_b16 v126, v0 offset:3664
	v_cvt_pk_bf16_f32 v0, v151, s0
	ds_write_b16 v126, v0 offset:3936
	v_cvt_pk_bf16_f32 v0, v33, s0
	ds_write_b16 v126, v0 offset:4208
	v_cvt_pk_bf16_f32 v0, v13, s0
	ds_write_b16 v126, v0 offset:192
	v_cvt_pk_bf16_f32 v0, v57, s0
	ds_write_b16 v126, v0 offset:464
	v_cvt_pk_bf16_f32 v0, v56, s0
	ds_write_b16 v126, v0 offset:736
	v_cvt_pk_bf16_f32 v0, v59, s0
	ds_write_b16 v126, v0 offset:1008
	v_cvt_pk_bf16_f32 v0, v58, s0
	ds_write_b16 v126, v0 offset:1280
	v_cvt_pk_bf16_f32 v0, v21, s0
	ds_write_b16 v126, v0 offset:1552
	v_cvt_pk_bf16_f32 v0, v60, s0
	ds_write_b16 v126, v0 offset:1824
	v_cvt_pk_bf16_f32 v0, v23, s0
	ds_write_b16 v126, v0 offset:2096
	v_cvt_pk_bf16_f32 v0, v8, s0
	ds_write_b16 v126, v0 offset:2368
	v_cvt_pk_bf16_f32 v0, v24, s0
	ds_write_b16 v126, v0 offset:2640
	v_cvt_pk_bf16_f32 v0, v25, s0
	ds_write_b16 v126, v0 offset:2912
	v_cvt_pk_bf16_f32 v0, v27, s0
	ds_write_b16 v126, v0 offset:3184
	v_cvt_pk_bf16_f32 v0, v122, s0
	ds_write_b16 v126, v0 offset:3456
	v_cvt_pk_bf16_f32 v0, v29, s0
	ds_write_b16 v126, v0 offset:3728
	v_cvt_pk_bf16_f32 v0, v130, s0
	ds_write_b16 v126, v0 offset:4000
	v_cvt_pk_bf16_f32 v0, v17, s0
	ds_write_b16 v126, v0 offset:4272
	s_waitcnt lgkmcnt(0)
; #define LAS __attribute__((address_space(3)))
; template <bool FINAL>
; __device__ __forceinline__ void s5_group(int lane, const unsigned char* tab, const bf16* __restrict__ proj, f32x2* E, int c, int g, LAS bf16* sbuf, LAS bf16* yg) {
;     ...
;             f32x16 y = (f32x16){};
;             const LAS bf16* sr = sbuf + r32 * SB_PITCH + 8 * hi; const bf16* cr_ = cmat + r32 * CM_PITCH + 8 * hi;
; #pragma unroll
;             for (int ks = 0; ks < 8; ++ks) { const bf16x8 afr = *(const LAS bf16x8*)(sr + 16 * ks); const bf16x8 cfr = *(const bf16x8*)(cr_ + 16 * ks);
;                 y = __builtin_amdgcn_mfma_f32_32x32x16_bf16(afr, cfr, y, 0, 0, 0); }
;             { const bf16x8 afr = tt ? dfr1 : dfr0; const bf16x8 cfr = *(const bf16x8*)(cr_ + 128);
;               y = __builtin_amdgcn_mfma_f32_32x32x16_bf16(afr, cfr, y, 0, 0, 0); }
	ds_read_b128 v[4:7], v128
	ds_read_b128 v[24:27], v128 offset:32
	s_waitcnt vmcnt(2) lgkmcnt(1)
	v_mfma_f32_32x32x16_bf16 v[0:15], v[4:7], v[164:167], 0
	s_waitcnt vmcnt(1) lgkmcnt(0)
	v_mfma_f32_32x32x16_bf16 v[0:15], v[24:27], v[168:171], v[0:15]
	ds_read_b128 v[24:27], v128 offset:64
	ds_read_b128 v[36:39], v128 offset:96
	s_waitcnt vmcnt(1) lgkmcnt(1)
	v_mfma_f32_32x32x16_bf16 v[0:15], v[24:27], v[172:175], v[0:15]
	s_waitcnt vmcnt(1) lgkmcnt(0)
	v_mfma_f32_32x32x16_bf16 v[0:15], v[36:39], v[176:179], v[0:15]
	ds_read_b128 v[28:31], v128 offset:128
	ds_read_b128 v[36:39], v128 offset:160
	s_waitcnt vmcnt(1) lgkmcnt(1)
	v_mfma_f32_32x32x16_bf16 v[0:15], v[28:31], v[180:183], v[0:15]
	s_waitcnt vmcnt(2) lgkmcnt(0)
	v_mfma_f32_32x32x16_bf16 v[0:15], v[36:39], v[184:187], v[0:15]
	ds_read_b128 v[20:23], v128 offset:192
	ds_read_b128 v[36:39], v128 offset:224
	s_waitcnt vmcnt(1) lgkmcnt(1)
	v_mfma_f32_32x32x16_bf16 v[0:15], v[20:23], v[188:191], v[0:15]
	v_cndmask_b32_e64 v27, v93, v89, s[8:9]
	v_cndmask_b32_e64 v26, v92, v88, s[8:9]
	v_cndmask_b32_e64 v25, v91, v87, s[8:9]
	v_cndmask_b32_e64 v24, v90, v86, s[8:9]
	s_waitcnt vmcnt(1) lgkmcnt(0)
	v_mfma_f32_32x32x16_bf16 v[0:15], v[36:39], v[228:231], v[0:15]
	s_waitcnt vmcnt(0)
	v_mfma_f32_32x32x16_bf16 v[0:15], v[24:27], v[232:235], v[0:15]
	s_and_saveexec_b64 s[10:11], s[38:39]
	s_cbranch_execz .LBB0_653
; #define LAS __attribute__((address_space(3)))
; __device__ __forceinline__ unsigned f2bf(float f) { return hw_pk_bf16(f, 0.f) & 0xffffu; }
; __device__ __forceinline__ float gelu_tanh(float x) {
;     const float u = 0.7978845608028654f * (x + 0.044715f * x * x * x);
;     const float e = __expf(2.0f * u);
;     return x - x * __builtin_amdgcn_rcpf(e + 1.0f);
; }
; template <bool FINAL>
; __device__ __forceinline__ void s5_group(int lane, const unsigned char* tab, const bf16* __restrict__ proj, f32x2* E, int c, int g, LAS bf16* sbuf, LAS bf16* yg) {
;     ...
;             if (r32 < 16) { LAS bf16* yw = yg + (32 * tt + 4 * hi) * YG_PITCH + 16 * g + r32;
; #pragma unroll
;                 for (int r = 0; r < 16; ++r) yw[((r & 3) + 8 * (r >> 2)) * YG_PITCH] = (bf16)f2bf(gelu_tanh(y[r])); }
;             asm volatile("s_waitcnt lgkmcnt(0)" ::: "memory");
	s_nop 9
	v_mul_f32_e32 v21, 0x3d372713, v0
	v_mul_f32_e32 v21, v0, v21
	v_fma_f32 v21, v0, v21, v0
	v_mul_f32_e32 v21, 0x3f4c422a, v21
	v_add_f32_e32 v21, v21, v21
	v_mul_f32_e32 v21, 0x3fb8aa3b, v21
	v_exp_f32_e32 v21, v21
	v_add_u32_e32 v20, s31, v129
	v_add_f32_e32 v21, 1.0, v21
	v_rcp_f32_e32 v21, v21
	s_nop 0
	v_fma_f32 v0, -v0, v21, v0
	v_cvt_pk_bf16_f32 v0, v0, s0
	ds_write_b16 v20, v0
	v_mul_f32_e32 v0, 0x3d372713, v1
	v_mul_f32_e32 v0, v1, v0
	v_fma_f32 v0, v1, v0, v1
	v_mul_f32_e32 v0, 0x3f4c422a, v0
	v_add_f32_e32 v0, v0, v0
	v_mul_f32_e32 v0, 0x3fb8aa3b, v0
	v_exp_f32_e32 v0, v0
	s_nop 0
	v_add_f32_e32 v0, 1.0, v0
	v_rcp_f32_e32 v0, v0
	s_nop 0
	v_fma_f32 v0, -v1, v0, v1
	v_cvt_pk_bf16_f32 v0, v0, s0
	ds_write_b16 v20, v0 offset:1040
	v_mul_f32_e32 v0, 0x3d372713, v2
	v_mul_f32_e32 v0, v2, v0
	v_fma_f32 v0, v2, v0, v2
	v_mul_f32_e32 v0, 0x3f4c422a, v0
	v_add_f32_e32 v0, v0, v0
	v_mul_f32_e32 v0, 0x3fb8aa3b, v0
	v_exp_f32_e32 v0, v0
	s_nop 0
	v_add_f32_e32 v0, 1.0, v0
	v_rcp_f32_e32 v0, v0
	s_nop 0
	v_fma_f32 v0, -v2, v0, v2
	v_cvt_pk_bf16_f32 v0, v0, s0
	ds_write_b16 v20, v0 offset:2080
	v_mul_f32_e32 v0, 0x3d372713, v3
	v_mul_f32_e32 v0, v3, v0
	v_fma_f32 v0, v3, v0, v3
	v_mul_f32_e32 v0, 0x3f4c422a, v0
	v_add_f32_e32 v0, v0, v0
	v_mul_f32_e32 v0, 0x3fb8aa3b, v0
	v_exp_f32_e32 v0, v0
	s_nop 0
	v_add_f32_e32 v0, 1.0, v0
	v_rcp_f32_e32 v0, v0
	s_nop 0
	v_fma_f32 v0, -v3, v0, v3
	v_cvt_pk_bf16_f32 v0, v0, s0
	ds_write_b16 v20, v0 offset:3120
	v_mul_f32_e32 v0, 0x3d372713, v4
	v_mul_f32_e32 v0, v4, v0
	v_fma_f32 v0, v4, v0, v4
	v_mul_f32_e32 v0, 0x3f4c422a, v0
	v_add_f32_e32 v0, v0, v0
	v_mul_f32_e32 v0, 0x3fb8aa3b, v0
	v_exp_f32_e32 v0, v0
	s_nop 0
	v_add_f32_e32 v0, 1.0, v0
	v_rcp_f32_e32 v0, v0
	s_nop 0
	v_fma_f32 v0, -v4, v0, v4
	v_cvt_pk_bf16_f32 v0, v0, s0
	ds_write_b16 v20, v0 offset:8320
	v_mul_f32_e32 v0, 0x3d372713, v5
	v_mul_f32_e32 v0, v5, v0
	v_fma_f32 v0, v5, v0, v5
	v_mul_f32_e32 v0, 0x3f4c422a, v0
	v_add_f32_e32 v0, v0, v0
	v_mul_f32_e32 v0, 0x3fb8aa3b, v0
	v_exp_f32_e32 v0, v0
	s_nop 0
	v_add_f32_e32 v0, 1.0, v0
	v_rcp_f32_e32 v0, v0
	s_nop 0
	v_fma_f32 v0, -v5, v0, v5
	v_cvt_pk_bf16_f32 v0, v0, s0
	ds_write_b16 v20, v0 offset:9360
	v_mul_f32_e32 v0, 0x3d372713, v6
	v_mul_f32_e32 v0, v6, v0
	v_fma_f32 v0, v6, v0, v6
	v_mul_f32_e32 v0, 0x3f4c422a, v0
	v_add_f32_e32 v0, v0, v0
	v_mul_f32_e32 v0, 0x3fb8aa3b, v0
	v_exp_f32_e32 v0, v0
	s_nop 0
	v_add_f32_e32 v0, 1.0, v0
	v_rcp_f32_e32 v0, v0
	s_nop 0
	v_fma_f32 v0, -v6, v0, v6
	v_cvt_pk_bf16_f32 v0, v0, s0
	ds_write_b16 v20, v0 offset:10400
	v_mul_f32_e32 v0, 0x3d372713, v7
	v_mul_f32_e32 v0, v7, v0
	v_fma_f32 v0, v7, v0, v7
	v_mul_f32_e32 v0, 0x3f4c422a, v0
	v_add_f32_e32 v0, v0, v0
	v_mul_f32_e32 v0, 0x3fb8aa3b, v0
	v_exp_f32_e32 v0, v0
	s_nop 0
	v_add_f32_e32 v0, 1.0, v0
	v_rcp_f32_e32 v0, v0
	s_nop 0
	v_fma_f32 v0, -v7, v0, v7
	v_cvt_pk_bf16_f32 v0, v0, s0
	ds_write_b16 v20, v0 offset:11440
	v_mul_f32_e32 v0, 0x3d372713, v8
	v_mul_f32_e32 v0, v8, v0
	v_fma_f32 v0, v8, v0, v8
	v_mul_f32_e32 v0, 0x3f4c422a, v0
	v_add_f32_e32 v0, v0, v0
	v_mul_f32_e32 v0, 0x3fb8aa3b, v0
	v_exp_f32_e32 v0, v0
	s_nop 0
	v_add_f32_e32 v0, 1.0, v0
	v_rcp_f32_e32 v0, v0
	s_nop 0
	v_fma_f32 v0, -v8, v0, v8
	v_cvt_pk_bf16_f32 v0, v0, s0
	ds_write_b16 v20, v0 offset:16640
	v_mul_f32_e32 v0, 0x3d372713, v9
	v_mul_f32_e32 v0, v9, v0
	v_fma_f32 v0, v9, v0, v9
	v_mul_f32_e32 v0, 0x3f4c422a, v0
	v_add_f32_e32 v0, v0, v0
	v_mul_f32_e32 v0, 0x3fb8aa3b, v0
	v_exp_f32_e32 v0, v0
	s_nop 0
	v_add_f32_e32 v0, 1.0, v0
	v_rcp_f32_e32 v0, v0
	s_nop 0
	v_fma_f32 v0, -v9, v0, v9
	v_cvt_pk_bf16_f32 v0, v0, s0
	ds_write_b16 v20, v0 offset:17680
	v_mul_f32_e32 v0, 0x3d372713, v10
	v_mul_f32_e32 v0, v10, v0
	v_fma_f32 v0, v10, v0, v10
	v_mul_f32_e32 v0, 0x3f4c422a, v0
	v_add_f32_e32 v0, v0, v0
	v_mul_f32_e32 v0, 0x3fb8aa3b, v0
	v_exp_f32_e32 v0, v0
	s_nop 0
	v_add_f32_e32 v0, 1.0, v0
	v_rcp_f32_e32 v0, v0
	s_nop 0
	v_fma_f32 v0, -v10, v0, v10
	v_cvt_pk_bf16_f32 v0, v0, s0
	ds_write_b16 v20, v0 offset:18720
	v_mul_f32_e32 v0, 0x3d372713, v11
	v_mul_f32_e32 v0, v11, v0
	v_fma_f32 v0, v11, v0, v11
	v_mul_f32_e32 v0, 0x3f4c422a, v0
	v_add_f32_e32 v0, v0, v0
	v_mul_f32_e32 v0, 0x3fb8aa3b, v0
	v_exp_f32_e32 v0, v0
	s_nop 0
	v_add_f32_e32 v0, 1.0, v0
	v_rcp_f32_e32 v0, v0
	s_nop 0
	v_fma_f32 v0, -v11, v0, v11
	v_cvt_pk_bf16_f32 v0, v0, s0
	ds_write_b16 v20, v0 offset:19760
	v_mul_f32_e32 v0, 0x3d372713, v12
	v_mul_f32_e32 v0, v12, v0
	v_fma_f32 v0, v12, v0, v12
	v_mul_f32_e32 v0, 0x3f4c422a, v0
	v_add_f32_e32 v0, v0, v0
	v_mul_f32_e32 v0, 0x3fb8aa3b, v0
	v_exp_f32_e32 v0, v0
	s_nop 0
	v_add_f32_e32 v0, 1.0, v0
	v_rcp_f32_e32 v0, v0
	s_nop 0
	v_fma_f32 v0, -v12, v0, v12
	v_cvt_pk_bf16_f32 v0, v0, s0
	ds_write_b16 v20, v0 offset:24960
	v_mul_f32_e32 v0, 0x3d372713, v13
	v_mul_f32_e32 v0, v13, v0
	v_fma_f32 v0, v13, v0, v13
	v_mul_f32_e32 v0, 0x3f4c422a, v0
	v_add_f32_e32 v0, v0, v0
	v_mul_f32_e32 v0, 0x3fb8aa3b, v0
	v_exp_f32_e32 v0, v0
	s_nop 0
	v_add_f32_e32 v0, 1.0, v0
	v_rcp_f32_e32 v0, v0
	s_nop 0
	v_fma_f32 v0, -v13, v0, v13
	v_cvt_pk_bf16_f32 v0, v0, s0
	ds_write_b16 v20, v0 offset:26000
	v_mul_f32_e32 v0, 0x3d372713, v14
	v_mul_f32_e32 v0, v14, v0
	v_fma_f32 v0, v14, v0, v14
	v_mul_f32_e32 v0, 0x3f4c422a, v0
	v_add_f32_e32 v0, v0, v0
	v_mul_f32_e32 v0, 0x3fb8aa3b, v0
	v_exp_f32_e32 v0, v0
	s_nop 0
	v_add_f32_e32 v0, 1.0, v0
	v_rcp_f32_e32 v0, v0
	s_nop 0
	v_fma_f32 v0, -v14, v0, v14
	v_cvt_pk_bf16_f32 v0, v0, s0
	ds_write_b16 v20, v0 offset:27040
	v_mul_f32_e32 v0, 0x3d372713, v15
	v_mul_f32_e32 v0, v15, v0
	v_fma_f32 v0, v15, v0, v15
	v_mul_f32_e32 v0, 0x3f4c422a, v0
	v_add_f32_e32 v0, v0, v0
	v_mul_f32_e32 v0, 0x3fb8aa3b, v0
	v_exp_f32_e32 v0, v0
	s_nop 0
	v_add_f32_e32 v0, 1.0, v0
	v_rcp_f32_e32 v0, v0
	s_nop 0
	v_fma_f32 v0, -v15, v0, v15
	v_cvt_pk_bf16_f32 v0, v0, s0
	ds_write_b16 v20, v0 offset:28080
	s_branch .LBB0_653
